# agg2 node groups run on the XCD that produced their y/z rows; csr buckets ordered so that the 3 workgroups of a CU take consecutive buckets
# speedup vs baseline: 1.0708x; 1.0078x over previous
_Z10k_csr_agg1PKjPKiPiPtPjPK15HIP_vector_typeIjLj2EEPS7_SA_:
	s_and_b32 s3, s2, 7
	s_lshr_b32 s2, s2, 3
	s_cmpk_lt_u32 s2, 0x60
	s_cbranch_scc0 .Lcsr_qdone
	s_and_b32 s5, s2, 31
	s_lshr_b32 s2, s2, 5
	s_mul_i32 s5, s5, 3
	s_add_i32 s2, s2, s5
.Lcsr_qdone:
	s_mul_i32 s4, s3, 0x62
	s_add_i32 s3, s3, 1
	s_lshr_b32 s3, s3, 3
	s_add_i32 s2, s2, s4
	s_sub_i32 s2, s2, s3
	s_movk_i32 s3, 0x100
	v_cmp_gt_u32_e32 vcc, s3, v0
	v_mov_b32_e32 v12, 0
	v_mov_b32_e32 v14, 0
	s_and_saveexec_b64 s[4:5], vcc
	s_cbranch_execz .LBB1_2
	s_load_dwordx2 s[6:7], s[0:1], 0x8
	s_lshl_b32 s3, s2, 8
	v_or_b32_e32 v2, s3, v0
	s_addk_i32 s3, 0x100
	v_ashrrev_i32_e32 v3, 31, v2
	v_or_b32_e32 v4, s3, v0
	s_waitcnt lgkmcnt(0)
	v_lshl_add_u64 v[2:3], v[2:3], 2, s[6:7]
	v_ashrrev_i32_e32 v5, 31, v4
	v_lshl_add_u64 v[4:5], v[4:5], 2, s[6:7]
	global_load_dword v14, v[2:3], off
	global_load_dword v12, v[4:5], off

_Z6k_agg2PK15HIP_vector_typeIjLj2EEPKS_IjLj4EEPKtPKjPf:
	s_and_b32 s3, s2, 7
	s_lshr_b32 s4, s2, 3
	s_cmpk_lt_u32 s4, 0x100
	s_cbranch_scc1 .Lag_lo
	s_cmpk_eq_u32 s4, 0x186
	s_cbranch_scc1 .Lag_tail
	s_sub_i32 s4, s4, 0x100
	s_lshr_b32 s5, s4, 1
	s_lshl_b32 s5, s5, 4
	s_and_b32 s4, s4, 1
	s_lshl_b32 s3, s3, 1
	s_add_i32 s2, s5, s4
	s_add_i32 s2, s2, s3
	s_addk_i32 s2, 0x800
	s_branch .Lag_done
.Lag_tail:
	s_add_i32 s2, s3, 0xc30
	s_branch .Lag_done
.Lag_lo:
	s_lshr_b32 s5, s4, 2
	s_lshl_b32 s5, s5, 5
	s_and_b32 s4, s4, 3
	s_lshl_b32 s3, s3, 2
	s_add_i32 s2, s5, s4
	s_add_i32 s2, s2, s3
.Lag_done:
	v_lshrrev_b32_e32 v1, 4, v0
	v_lshl_or_b32 v6, s2, 4, v1
	s_mov_b32 s2, 0xc350
	v_cmp_gt_i32_e32 vcc, s2, v6
	s_and_saveexec_b64 s[2:3], vcc
	s_cbranch_execz .LBB3_14
	s_load_dwordx2 s[2:3], s[0:1], 0x18
	s_load_dwordx4 s[4:7], s[0:1], 0x0
	v_lshlrev_b32_e32 v2, 4, v6
	v_and_b32_e32 v48, 15, v0
	v_ashrrev_i32_e32 v3, 31, v2
	v_lshlrev_b32_e32 v12, 2, v48
	s_waitcnt lgkmcnt(0)
	v_lshl_add_u64 v[4:5], v[2:3], 2, s[2:3]
	v_mov_b32_e32 v13, 0
	v_lshl_add_u64 v[4:5], v[4:5], 0, v[12:13]
	global_load_dword v53, v[4:5], off nt
	v_or_b32_e32 v2, v2, v48
	v_ashrrev_i32_e32 v3, 31, v2
	v_lshl_add_u64 v[2:3], v[2:3], 4, s[6:7]
	global_load_dwordx4 v[2:5], v[2:3], off nt
	v_mbcnt_lo_u32_b32 v1, -1, 0
	v_mbcnt_hi_u32_b32 v7, -1, v1
	v_and_b32_e32 v0, 48, v0
	v_and_b32_e32 v49, 64, v7
	v_or_b32_e32 v51, v49, v0
	v_lshlrev_b32_e32 v54, 2, v51
	v_mov_b32_e32 v10, v13
	v_mov_b32_e32 v11, v13
	v_mov_b32_e32 v8, v13
	v_mov_b32_e32 v9, v13
	v_mov_b32_e32 v0, v13
	v_mov_b32_e32 v1, v13
	v_mov_b32_e32 v14, v13
	v_mov_b32_e32 v12, v13
	s_waitcnt vmcnt(1)
	ds_bpermute_b32 v15, v54, v53
	s_waitcnt lgkmcnt(0)
	v_and_b32_e32 v50, 0x7fffffff, v15
	v_min_u32_e32 v16, 24, v50
	v_cmp_lt_i32_e32 vcc, -1, v15
	v_mov_b32_e32 v15, v13
	s_nop 0
	v_cndmask_b32_e32 v52, 0, v16, vcc
	v_cmp_ne_u32_e32 vcc, 0, v52
	s_and_saveexec_b64 s[2:3], vcc
	s_cbranch_execz .LBB3_5
	ds_bpermute_b32 v0, v54, v53 offset:4
	ds_bpermute_b32 v1, v54, v53 offset:8
	s_mov_b32 s8, 0xffff0
	ds_bpermute_b32 v9, v54, v53 offset:12
	ds_bpermute_b32 v16, v54, v53 offset:20
	s_waitcnt lgkmcnt(3)
	v_lshlrev_b32_e32 v8, 4, v0
	v_and_or_b32 v8, v8, s8, v48
	v_lshlrev_b32_e32 v8, 3, v8
	v_bfe_u32 v0, v0, 16, 16
	global_load_dwordx2 v[34:35], v8, s[4:5]
	s_waitcnt lgkmcnt(2)
	v_lshlrev_b32_e32 v8, 4, v1
	v_bfe_u32 v1, v1, 16, 16
	v_lshl_or_b32 v0, v0, 4, v48
	v_lshl_or_b32 v1, v1, 4, v48
	v_lshlrev_b32_e32 v0, 3, v0
	v_and_or_b32 v8, v8, s8, v48
	v_lshlrev_b32_e32 v1, 3, v1
	v_lshlrev_b32_e32 v8, 3, v8
	global_load_dwordx2 v[36:37], v0, s[4:5]
	global_load_dwordx2 v[32:33], v8, s[4:5]
	global_load_dwordx2 v[12:13], v1, s[4:5]
	ds_bpermute_b32 v1, v54, v53 offset:16
	s_waitcnt lgkmcnt(2)
	v_bfe_u32 v8, v9, 16, 16
	v_lshl_or_b32 v8, v8, 4, v48
	ds_bpermute_b32 v17, v54, v53 offset:24
	v_lshlrev_b32_e32 v0, 4, v9
	v_lshlrev_b32_e32 v14, 3, v8
	s_waitcnt lgkmcnt(1)
	v_lshlrev_b32_e32 v8, 4, v1
	v_bfe_u32 v1, v1, 16, 16
	v_and_or_b32 v0, v0, s8, v48
	v_and_or_b32 v8, v8, s8, v48
	v_lshl_or_b32 v1, v1, 4, v48
	v_lshlrev_b32_e32 v0, 3, v0
	v_lshlrev_b32_e32 v15, 3, v8
	v_lshlrev_b32_e32 v1, 3, v1
	global_load_dwordx2 v[30:31], v0, s[4:5]
	global_load_dwordx2 v[10:11], v14, s[4:5]
	global_load_dwordx2 v[8:9], v15, s[4:5]
	s_nop 0
	global_load_dwordx2 v[0:1], v1, s[4:5]
	v_lshlrev_b32_e32 v14, 4, v16
	v_bfe_u32 v15, v16, 16, 16
	v_and_or_b32 v14, v14, s8, v48
	v_lshl_or_b32 v15, v15, 4, v48
	s_waitcnt lgkmcnt(0)
	v_lshlrev_b32_e32 v16, 4, v17
	v_lshlrev_b32_e32 v14, 3, v14
	v_lshlrev_b32_e32 v15, 3, v15
	v_and_or_b32 v16, v16, s8, v48
	v_lshlrev_b32_e32 v16, 3, v16
	global_load_dwordx2 v[22:23], v14, s[4:5]
	global_load_dwordx2 v[18:19], v15, s[4:5]
	s_nop 0
	global_load_dwordx2 v[14:15], v16, s[4:5]
	v_bfe_u32 v17, v17, 16, 16
	v_lshl_or_b32 v17, v17, 4, v48
	v_lshlrev_b32_e32 v17, 3, v17
	global_load_dwordx2 v[24:25], v17, s[4:5]
	ds_bpermute_b32 v16, v54, v53 offset:28
	v_cmp_lt_u32_e32 vcc, 16, v52
	s_waitcnt lgkmcnt(0)
	v_lshlrev_b32_e32 v17, 4, v16
	v_and_or_b32 v17, v17, s8, v48
	v_lshlrev_b32_e32 v17, 3, v17
	global_load_dwordx2 v[28:29], v17, s[4:5]
	ds_bpermute_b32 v17, v54, v53 offset:32
	v_bfe_u32 v16, v16, 16, 16
	v_lshl_or_b32 v16, v16, 4, v48
	v_lshlrev_b32_e32 v16, 3, v16
	s_waitcnt lgkmcnt(0)
	v_lshlrev_b32_e32 v20, 4, v17
	v_bfe_u32 v17, v17, 16, 16
	v_and_or_b32 v20, v20, s8, v48
	v_lshl_or_b32 v17, v17, 4, v48
	v_lshlrev_b32_e32 v20, 3, v20
	v_lshlrev_b32_e32 v17, 3, v17
	global_load_dwordx2 v[26:27], v16, s[4:5]
	s_nop 0
	global_load_dwordx2 v[20:21], v20, s[4:5]
	s_nop 0
	global_load_dwordx2 v[16:17], v17, s[4:5]
	s_waitcnt vmcnt(15)
	v_cvt_pk_f32_fp8_e32 v[38:39], v34
	v_cvt_pk_f32_fp8_sdwa v[42:43], v34 src0_sel:WORD_1
	v_cvt_pk_f32_fp8_e32 v[44:45], v35
	v_cvt_pk_f32_fp8_sdwa v[34:35], v35 src0_sel:WORD_1
	s_waitcnt vmcnt(14)
	v_cvt_pk_f32_fp8_sdwa v[58:59], v36 src0_sel:WORD_1
	v_cvt_pk_f32_fp8_e32 v[56:57], v36
	v_cvt_pk_f32_fp8_e32 v[60:61], v37
	v_cvt_pk_f32_fp8_sdwa v[62:63], v37 src0_sel:WORD_1
	s_waitcnt vmcnt(13)
	v_cvt_pk_f32_fp8_e32 v[46:47], v32
	v_pk_add_f32 v[36:37], v[38:39], 0 op_sel_hi:[1,0]
	v_pk_add_f32 v[38:39], v[42:43], 0 op_sel_hi:[1,0]
	v_pk_add_f32 v[56:57], v[36:37], v[56:57]
	v_pk_add_f32 v[42:43], v[38:39], v[58:59]
	s_waitcnt vmcnt(12)
	v_cvt_pk_f32_fp8_e32 v[58:59], v12
	v_pk_add_f32 v[38:39], v[44:45], 0 op_sel_hi:[1,0]
	v_pk_add_f32 v[46:47], v[56:57], v[46:47]
	v_pk_add_f32 v[38:39], v[38:39], v[60:61]
	s_waitcnt vmcnt(11)
	v_cvt_pk_f32_fp8_e32 v[60:61], v30
	s_waitcnt vmcnt(10)
	v_cvt_pk_f32_fp8_e32 v[56:57], v10
	v_pk_add_f32 v[46:47], v[46:47], v[58:59]
	s_waitcnt vmcnt(9)
	v_cvt_pk_f32_fp8_e32 v[58:59], v8
	v_pk_add_f32 v[46:47], v[46:47], v[60:61]
	s_waitcnt vmcnt(8)
	v_cvt_pk_f32_fp8_e32 v[60:61], v0
	v_pk_add_f32 v[46:47], v[46:47], v[56:57]
	v_cvt_pk_f32_fp8_sdwa v[40:41], v32 src0_sel:WORD_1
	v_pk_add_f32 v[46:47], v[46:47], v[58:59]
	v_cvt_pk_f32_fp8_sdwa v[44:45], v12 src0_sel:WORD_1
	v_pk_add_f32 v[46:47], v[46:47], v[60:61]
	v_pk_add_f32 v[40:41], v[42:43], v[40:41]
	s_waitcnt vmcnt(7)
	v_cvt_pk_f32_fp8_e32 v[56:57], v22
	s_waitcnt vmcnt(6)
	v_cvt_pk_f32_fp8_e32 v[58:59], v18
	s_waitcnt vmcnt(5)
	v_cvt_pk_f32_fp8_e32 v[60:61], v14
	v_cvt_pk_f32_fp8_sdwa v[42:43], v10 src0_sel:WORD_1
	v_pk_add_f32 v[46:47], v[46:47], v[56:57]
	v_cvt_pk_f32_fp8_e32 v[56:57], v13
	v_pk_add_f32 v[46:47], v[46:47], v[58:59]
	s_waitcnt vmcnt(4)
	v_cvt_pk_f32_fp8_e32 v[58:59], v24
	v_pk_add_f32 v[60:61], v[46:47], v[60:61]
	v_cvt_pk_f32_fp8_sdwa v[46:47], v13 src0_sel:WORD_1
	v_pk_add_f32 v[40:41], v[40:41], v[44:45]
	v_pk_add_f32 v[12:13], v[60:61], v[58:59]
	v_cvt_pk_f32_fp8_sdwa v[58:59], v30 src0_sel:WORD_1
	v_cvt_pk_f32_fp8_sdwa v[44:45], v8 src0_sel:WORD_1
	v_cvt_pk_f32_fp8_e32 v[36:37], v33
	v_cvt_pk_f32_fp8_sdwa v[32:33], v33 src0_sel:WORD_1
	v_pk_add_f32 v[40:41], v[40:41], v[58:59]
	v_cvt_pk_f32_fp8_sdwa v[58:59], v0 src0_sel:WORD_1
	v_pk_add_f32 v[40:41], v[40:41], v[42:43]
	v_cvt_pk_f32_fp8_sdwa v[42:43], v22 src0_sel:WORD_1
	v_pk_add_f32 v[40:41], v[40:41], v[44:45]
	v_cvt_pk_f32_fp8_sdwa v[44:45], v18 src0_sel:WORD_1
	v_pk_add_f32 v[40:41], v[40:41], v[58:59]
	v_pk_add_f32 v[34:35], v[34:35], 0 op_sel_hi:[1,0]
	v_pk_add_f32 v[40:41], v[40:41], v[42:43]
	v_cvt_pk_f32_fp8_sdwa v[42:43], v14 src0_sel:WORD_1
	v_pk_add_f32 v[40:41], v[40:41], v[44:45]
	v_cvt_pk_f32_fp8_sdwa v[44:45], v24 src0_sel:WORD_1
	v_cvt_pk_f32_fp8_e32 v[60:61], v31
	v_pk_add_f32 v[40:41], v[40:41], v[42:43]
	s_waitcnt vmcnt(3)
	v_cvt_pk_f32_fp8_sdwa v[42:43], v28 src0_sel:WORD_1
	v_cvt_pk_f32_fp8_sdwa v[30:31], v31 src0_sel:WORD_1
	v_pk_add_f32 v[34:35], v[34:35], v[62:63]
	v_cvt_pk_f32_fp8_e32 v[58:59], v11
	v_cvt_pk_f32_fp8_sdwa v[10:11], v11 src0_sel:WORD_1
	v_pk_add_f32 v[40:41], v[40:41], v[44:45]
	v_cvt_pk_f32_fp8_e32 v[44:45], v9
	v_cvt_pk_f32_fp8_sdwa v[8:9], v9 src0_sel:WORD_1
	v_pk_add_f32 v[32:33], v[34:35], v[32:33]
	v_pk_add_f32 v[40:41], v[40:41], v[42:43]
	v_cvt_pk_f32_fp8_e32 v[42:43], v1
	v_cvt_pk_f32_fp8_sdwa v[0:1], v1 src0_sel:WORD_1
	v_pk_add_f32 v[32:33], v[32:33], v[46:47]
	v_pk_add_f32 v[36:37], v[38:39], v[36:37]
	v_cvt_pk_f32_fp8_e32 v[38:39], v23
	v_cvt_pk_f32_fp8_sdwa v[22:23], v23 src0_sel:WORD_1
	v_pk_add_f32 v[30:31], v[32:33], v[30:31]
	v_pk_add_f32 v[36:37], v[36:37], v[56:57]
	v_cvt_pk_f32_fp8_e32 v[56:57], v19
	v_cvt_pk_f32_fp8_sdwa v[18:19], v19 src0_sel:WORD_1
	v_pk_add_f32 v[10:11], v[30:31], v[10:11]
	v_pk_add_f32 v[36:37], v[36:37], v[60:61]
	v_cvt_pk_f32_fp8_e32 v[60:61], v15
	v_cvt_pk_f32_fp8_sdwa v[14:15], v15 src0_sel:WORD_1
	v_pk_add_f32 v[8:9], v[10:11], v[8:9]
	v_pk_add_f32 v[36:37], v[36:37], v[58:59]
	v_cvt_pk_f32_fp8_e32 v[58:59], v25
	v_cvt_pk_f32_fp8_sdwa v[24:25], v25 src0_sel:WORD_1
	v_pk_add_f32 v[0:1], v[8:9], v[0:1]
	v_cvt_pk_f32_fp8_e32 v[62:63], v28
	v_pk_add_f32 v[36:37], v[36:37], v[44:45]
	v_cvt_pk_f32_fp8_e32 v[44:45], v29
	v_cvt_pk_f32_fp8_sdwa v[28:29], v29 src0_sel:WORD_1
	v_pk_add_f32 v[0:1], v[0:1], v[22:23]
	s_waitcnt vmcnt(1)
	v_cvt_pk_f32_fp8_e32 v[10:11], v20
	v_pk_add_f32 v[0:1], v[0:1], v[18:19]
	v_pk_add_f32 v[36:37], v[36:37], v[42:43]
	v_pk_add_f32 v[0:1], v[0:1], v[14:15]
	v_cvt_pk_f32_fp8_sdwa v[8:9], v26 src0_sel:WORD_1
	v_pk_add_f32 v[0:1], v[0:1], v[24:25]
	v_pk_add_f32 v[12:13], v[12:13], v[62:63]
	v_pk_add_f32 v[14:15], v[0:1], v[28:29]
	v_cvt_pk_f32_fp8_e32 v[0:1], v26
	s_waitcnt vmcnt(0)
	v_cvt_pk_f32_fp8_e32 v[28:29], v16
	v_pk_add_f32 v[36:37], v[36:37], v[38:39]
	v_cvt_pk_f32_fp8_sdwa v[22:23], v27 src0_sel:WORD_1
	v_cvt_pk_f32_fp8_sdwa v[24:25], v20 src0_sel:WORD_1
	v_pk_add_f32 v[36:37], v[36:37], v[56:57]
	v_cvt_pk_f32_fp8_e32 v[18:19], v27
	v_cvt_pk_f32_fp8_e32 v[26:27], v21
	v_cvt_pk_f32_fp8_sdwa v[20:21], v21 src0_sel:WORD_1
	v_cvt_pk_f32_fp8_sdwa v[30:31], v16 src0_sel:WORD_1
	v_pk_add_f32 v[0:1], v[12:13], v[0:1]
	v_pk_add_f32 v[36:37], v[36:37], v[60:61]
	v_cvt_pk_f32_fp8_e32 v[32:33], v17
	v_cvt_pk_f32_fp8_sdwa v[16:17], v17 src0_sel:WORD_1
	v_pk_add_f32 v[0:1], v[0:1], v[10:11]
	v_pk_add_f32 v[36:37], v[36:37], v[58:59]
	v_pk_add_f32 v[10:11], v[0:1], v[28:29]
	v_pk_add_f32 v[0:1], v[40:41], v[8:9]
	v_pk_add_f32 v[36:37], v[36:37], v[44:45]
	v_pk_add_f32 v[0:1], v[0:1], v[24:25]
	v_pk_add_f32 v[12:13], v[14:15], v[22:23]
	v_pk_add_f32 v[8:9], v[0:1], v[30:31]
	v_pk_add_f32 v[0:1], v[36:37], v[18:19]
	v_pk_add_f32 v[12:13], v[12:13], v[20:21]
	v_pk_add_f32 v[0:1], v[0:1], v[26:27]
	v_pk_add_f32 v[12:13], v[12:13], v[16:17]
	v_pk_add_f32 v[0:1], v[0:1], v[32:33]
	v_mov_b32_e32 v15, v13
	v_mov_b32_e32 v14, v12
	s_and_saveexec_b64 s[6:7], vcc
	s_cbranch_execz .LBB3_4
	ds_bpermute_b32 v14, v54, v53 offset:36
	ds_bpermute_b32 v15, v54, v53 offset:40
	ds_bpermute_b32 v16, v54, v53 offset:44
	s_waitcnt lgkmcnt(2)
	v_lshlrev_b32_e32 v17, 4, v14
	v_bfe_u32 v14, v14, 16, 16
	v_and_or_b32 v17, v17, s8, v48
	v_lshl_or_b32 v14, v14, 4, v48
	v_lshlrev_b32_e32 v17, 3, v17
	v_lshlrev_b32_e32 v14, 3, v14
	global_load_dwordx2 v[20:21], v17, s[4:5]
	global_load_dwordx2 v[22:23], v14, s[4:5]
	s_waitcnt lgkmcnt(1)
	v_lshlrev_b32_e32 v14, 4, v15
	v_and_or_b32 v14, v14, s8, v48
	v_lshlrev_b32_e32 v14, 3, v14
	global_load_dwordx2 v[24:25], v14, s[4:5]
	v_bfe_u32 v14, v15, 16, 16
	s_waitcnt lgkmcnt(0)
	v_bfe_u32 v15, v16, 16, 16
	v_lshl_or_b32 v14, v14, 4, v48
	v_lshl_or_b32 v15, v15, 4, v48
	v_lshlrev_b32_e32 v14, 3, v14
	v_lshlrev_b32_e32 v15, 3, v15
	global_load_dwordx2 v[26:27], v14, s[4:5]
	global_load_dwordx2 v[18:19], v15, s[4:5]
	v_lshlrev_b32_e32 v14, 4, v16
	v_and_or_b32 v14, v14, s8, v48
	v_lshlrev_b32_e32 v14, 3, v14
	global_load_dwordx2 v[28:29], v14, s[4:5]
	ds_bpermute_b32 v14, v54, v53 offset:48
	s_waitcnt lgkmcnt(0)
	v_lshlrev_b32_e32 v15, 4, v14
	v_and_or_b32 v15, v15, s8, v48
	v_bfe_u32 v14, v14, 16, 16
	v_lshlrev_b32_e32 v15, 3, v15
	v_lshl_or_b32 v14, v14, 4, v48
	global_load_dwordx2 v[16:17], v15, s[4:5]
	v_lshlrev_b32_e32 v14, 3, v14
	global_load_dwordx2 v[14:15], v14, s[4:5]
	s_waitcnt vmcnt(7)
	v_cvt_pk_f32_fp8_e32 v[30:31], v20
	v_cvt_pk_f32_fp8_sdwa v[32:33], v20 src0_sel:WORD_1
	v_cvt_pk_f32_fp8_e32 v[34:35], v21
	v_cvt_pk_f32_fp8_sdwa v[20:21], v21 src0_sel:WORD_1
	s_waitcnt vmcnt(6)
	v_cvt_pk_f32_fp8_e32 v[36:37], v22
	v_cvt_pk_f32_fp8_sdwa v[38:39], v22 src0_sel:WORD_1
	v_cvt_pk_f32_fp8_e32 v[40:41], v23
	v_cvt_pk_f32_fp8_sdwa v[22:23], v23 src0_sel:WORD_1
	s_waitcnt vmcnt(5)
	v_cvt_pk_f32_fp8_e32 v[42:43], v24
	v_cvt_pk_f32_fp8_sdwa v[44:45], v24 src0_sel:WORD_1
	v_cvt_pk_f32_fp8_e32 v[46:47], v25
	v_cvt_pk_f32_fp8_sdwa v[24:25], v25 src0_sel:WORD_1
	s_waitcnt vmcnt(4)
	v_cvt_pk_f32_fp8_e32 v[54:55], v26
	v_cvt_pk_f32_fp8_sdwa v[56:57], v26 src0_sel:WORD_1
	v_cvt_pk_f32_fp8_e32 v[58:59], v27
	v_cvt_pk_f32_fp8_sdwa v[26:27], v27 src0_sel:WORD_1
	v_pk_add_f32 v[10:11], v[10:11], v[30:31]
	s_waitcnt vmcnt(2)
	v_cvt_pk_f32_fp8_e32 v[60:61], v28
	v_cvt_pk_f32_fp8_sdwa v[30:31], v28 src0_sel:WORD_1
	v_pk_add_f32 v[8:9], v[8:9], v[32:33]
	v_cvt_pk_f32_fp8_e32 v[32:33], v29
	v_cvt_pk_f32_fp8_sdwa v[28:29], v29 src0_sel:WORD_1
	v_pk_add_f32 v[12:13], v[12:13], v[20:21]
	v_pk_add_f32 v[0:1], v[0:1], v[34:35]
	v_cvt_pk_f32_fp8_e32 v[34:35], v18
	v_cvt_pk_f32_fp8_sdwa v[20:21], v18 src0_sel:WORD_1
	v_pk_add_f32 v[10:11], v[10:11], v[36:37]
	v_cvt_pk_f32_fp8_e32 v[36:37], v19
	v_cvt_pk_f32_fp8_sdwa v[18:19], v19 src0_sel:WORD_1
	v_pk_add_f32 v[12:13], v[12:13], v[22:23]
	v_pk_add_f32 v[8:9], v[8:9], v[38:39]
	s_waitcnt vmcnt(1)
	v_cvt_pk_f32_fp8_e32 v[38:39], v16
	v_pk_add_f32 v[0:1], v[0:1], v[40:41]
	v_cvt_pk_f32_fp8_sdwa v[40:41], v16 src0_sel:WORD_1
	v_cvt_pk_f32_fp8_e32 v[22:23], v17
	v_cvt_pk_f32_fp8_sdwa v[16:17], v17 src0_sel:WORD_1
	v_pk_add_f32 v[12:13], v[12:13], v[24:25]
	v_pk_add_f32 v[10:11], v[10:11], v[42:43]
	s_waitcnt vmcnt(0)
	v_cvt_pk_f32_fp8_e32 v[42:43], v14
	v_pk_add_f32 v[8:9], v[8:9], v[44:45]
	v_cvt_pk_f32_fp8_sdwa v[44:45], v14 src0_sel:WORD_1
	v_pk_add_f32 v[0:1], v[0:1], v[46:47]
	v_cvt_pk_f32_fp8_e32 v[46:47], v15
	v_cvt_pk_f32_fp8_sdwa v[14:15], v15 src0_sel:WORD_1
	v_pk_add_f32 v[12:13], v[12:13], v[26:27]
	v_pk_add_f32 v[10:11], v[10:11], v[54:55]
	v_pk_add_f32 v[8:9], v[8:9], v[56:57]
	v_pk_add_f32 v[0:1], v[0:1], v[58:59]
	v_pk_add_f32 v[12:13], v[12:13], v[28:29]
	v_pk_add_f32 v[10:11], v[10:11], v[60:61]
	v_pk_add_f32 v[8:9], v[8:9], v[30:31]
	v_pk_add_f32 v[0:1], v[0:1], v[32:33]
	v_pk_add_f32 v[12:13], v[12:13], v[18:19]
	v_pk_add_f32 v[10:11], v[10:11], v[34:35]
	v_pk_add_f32 v[8:9], v[8:9], v[20:21]
	v_pk_add_f32 v[0:1], v[0:1], v[36:37]
	v_pk_add_f32 v[12:13], v[12:13], v[16:17]
	v_pk_add_f32 v[10:11], v[10:11], v[38:39]
	v_pk_add_f32 v[8:9], v[8:9], v[40:41]
	v_pk_add_f32 v[0:1], v[0:1], v[22:23]
	v_pk_add_f32 v[14:15], v[12:13], v[14:15]
	v_pk_add_f32 v[10:11], v[10:11], v[42:43]
	v_pk_add_f32 v[8:9], v[8:9], v[44:45]
	v_pk_add_f32 v[0:1], v[0:1], v[46:47]
	v_mov_b64_e32 v[12:13], v[14:15]
